# speedup vs baseline: 1.0119x; 1.0119x over previous
.LBB0_3:
	v_and_b32_e32 v38, 0x7c, v127
	v_lshlrev_b32_e32 v66, 2, v38
	v_mov_b32_e32 v67, 0
	v_lshlrev_b32_e32 v38, 5, v131
	v_lshl_add_u64 v[68:69], s[8:9], 0, v[66:67]
	v_and_b32_e32 v66, 0x1fc00, v38
	v_lshlrev_b32_e32 v38, 5, v132
	v_lshl_add_u64 v[46:47], v[68:69], 0, v[66:67]
	v_and_b32_e32 v66, 0x1fc00, v38
	v_lshl_add_u64 v[48:49], v[68:69], 0, v[66:67]
	global_load_dwordx4 v[38:41], v[46:47], off
	global_load_dwordx4 v[42:45], v[48:49], off
	v_lshlrev_b32_e32 v46, 5, v133
	v_and_b32_e32 v66, 0x1fc00, v46
	v_lshlrev_b32_e32 v46, 5, v134
	v_lshl_add_u64 v[54:55], v[68:69], 0, v[66:67]
	v_and_b32_e32 v66, 0x1fc00, v46
	v_lshl_add_u64 v[56:57], v[68:69], 0, v[66:67]
	global_load_dwordx4 v[46:49], v[54:55], off
	global_load_dwordx4 v[50:53], v[56:57], off
	v_lshlrev_b32_e32 v54, 5, v135
	v_and_b32_e32 v66, 0x1fc00, v54
	v_lshlrev_b32_e32 v54, 5, v136
	v_lshl_add_u64 v[62:63], v[68:69], 0, v[66:67]
	v_and_b32_e32 v66, 0x1fc00, v54
	v_lshl_add_u64 v[64:65], v[68:69], 0, v[66:67]
	global_load_dwordx4 v[54:57], v[62:63], off
	global_load_dwordx4 v[58:61], v[64:65], off
	v_lshlrev_b32_e32 v62, 5, v137
	v_and_b32_e32 v66, 0x1fc00, v62
	v_lshl_add_u64 v[62:63], v[68:69], 0, v[66:67]
	v_lshlrev_b32_e32 v66, 5, v138
	v_and_b32_e32 v66, 0x1fc00, v66
	v_lshl_add_u64 v[66:67], v[68:69], 0, v[66:67]
	global_load_dwordx4 v[62:65], v[62:63], off
	s_waitcnt vmcnt(6)
	v_cvt_pk_bf16_f32 v110, v38, v39
	global_load_dwordx4 v[66:69], v[66:67], off
	v_cvt_pk_bf16_f32 v111, v40, v41
	s_waitcnt vmcnt(6)
	v_cvt_pk_bf16_f32 v112, v42, v43
	v_cvt_pk_bf16_f32 v113, v44, v45
	s_waitcnt vmcnt(5)
	v_cvt_pk_bf16_f32 v114, v46, v47
	v_cvt_pk_bf16_f32 v115, v48, v49
	s_waitcnt vmcnt(4)
	v_cvt_pk_bf16_f32 v116, v50, v51
	v_cvt_pk_bf16_f32 v117, v52, v53
	s_waitcnt vmcnt(3)
	v_cvt_pk_bf16_f32 v118, v54, v55
	v_cvt_pk_bf16_f32 v119, v56, v57
	s_waitcnt vmcnt(2)
	v_cvt_pk_bf16_f32 v120, v58, v59
	v_cvt_pk_bf16_f32 v121, v60, v61
	s_waitcnt vmcnt(1)
	v_cvt_pk_bf16_f32 v122, v62, v63
	v_cvt_pk_bf16_f32 v123, v64, v65
	s_waitcnt vmcnt(0)
	v_cvt_pk_bf16_f32 v124, v66, v67
	v_cvt_pk_bf16_f32 v125, v68, v69

.LBB0_14:
	v_and_b32_e32 v26, 48, v0
	v_mad_u32_u24 v48, v1, s8, v26
	v_add_u32_e32 v24, 0x1b400, v48
	ds_read_b128 v[18:21], v24
	v_mad_u32_u24 v49, v107, s8, v26
	ds_read_b128 v[28:31], v49
	ds_read_b128 v[32:35], v24 offset:64
	ds_read_b128 v[36:39], v49 offset:64
	v_lshlrev_b32_e32 v25, 1, v107
	s_mov_b32 s5, 0x1c500
	s_and_b64 vcc, exec, s[6:7]
	s_waitcnt lgkmcnt(2)
	v_mfma_f32_16x16x32_bf16 v[18:21], v[18:21], v[28:31], 0
	ds_read_b128 v[28:31], v24 offset:128
	ds_read_b128 v[40:43], v49 offset:128
	ds_read_b128 v[44:47], v24 offset:192
	v_lshrrev_b32_e32 v24, 4, v126
	v_mul_u32_u24_e32 v27, 0x440, v24
	s_waitcnt lgkmcnt(3)
	v_mfma_f32_16x16x32_bf16 v[18:21], v[32:35], v[36:39], v[18:21]
	ds_read_b128 v[32:35], v49 offset:192
	s_waitcnt lgkmcnt(2)
	v_mfma_f32_16x16x32_bf16 v[18:21], v[28:31], v[40:43], v[18:21]
	v_add3_u32 v28, v27, v25, s5
	v_add_u32_e32 v40, 0x1c500, v48
	s_waitcnt lgkmcnt(0)
	v_mfma_f32_16x16x32_bf16 v[18:21], v[44:47], v[32:35], v[18:21]
	s_nop 7
	v_mul_f32_e32 v18, s4, v18
	v_mul_f32_e32 v19, s4, v19
	v_mul_f32_e32 v20, s4, v20
	v_mul_f32_e32 v21, s4, v21
	v_cvt_pk_bf16_f32 v18, v18, s0
	v_cvt_pk_bf16_f32 v19, v19, s0
	v_cvt_pk_bf16_f32 v20, v20, s0
	ds_write_b16 v28, v18
	ds_write_b16 v28, v19 offset:272
	ds_write_b16 v28, v20 offset:544
	v_cvt_pk_bf16_f32 v18, v21, s0
	ds_write_b16 v28, v18 offset:816
	s_waitcnt lgkmcnt(0)
	s_barrier
	ds_read_b128 v[18:21], v40
	ds_read_b128 v[28:31], v40 offset:64
	ds_read_b128 v[32:35], v49 offset:34816
	ds_read_b128 v[36:39], v49 offset:34880
	s_waitcnt lgkmcnt(1)
	v_mfma_f32_16x16x32_bf16 v[18:21], v[18:21], v[32:35], 0
	ds_read_b128 v[32:35], v40 offset:128
	ds_read_b128 v[40:43], v40 offset:192
	s_mov_b64 s[4:5], -1
	s_waitcnt lgkmcnt(2)
	v_mfma_f32_16x16x32_bf16 v[18:21], v[28:31], v[36:39], v[18:21]
	ds_read_b128 v[28:31], v49 offset:34944
	ds_read_b128 v[36:39], v49 offset:35008
	s_waitcnt lgkmcnt(1)
	v_mfma_f32_16x16x32_bf16 v[18:21], v[32:35], v[28:31], v[18:21]
	s_waitcnt lgkmcnt(0)
	v_mfma_f32_16x16x32_bf16 v[18:21], v[40:43], v[36:39], v[18:21]
	s_cbranch_vccz .LBB0_24
	v_or_b32_e32 v28, 0x1d600, v106
	ds_read_b32 v28, v28
	s_load_dwordx2 s[4:5], s[0:1], 0x70
	v_lshl_or_b32 v30, v24, 2, s3
	v_ashrrev_i32_e32 v31, 31, v30
	v_mov_b32_e32 v107, 0
	s_waitcnt lgkmcnt(0)
	v_add_f32_e32 v34, v130, v28
	v_add_f32_e32 v35, v34, v18
	v_add_f32_e32 v28, v35, v35
	v_mul_f32_e32 v28, 0x3fb8aa3b, v28
	v_exp_f32_e32 v32, v28
	v_lshlrev_b64 v[28:29], 9, v[30:31]
	s_mov_b32 s8, 0x19200
	v_add3_u32 v37, v27, v25, s8
	v_add_f32_e32 v31, 1.0, v32
	v_rcp_f32_e32 v31, v31
	v_lshl_add_u64 v[32:33], s[4:5], 0, v[106:107]
	v_lshl_add_u64 v[28:29], v[32:33], 0, v[28:29]
	global_store_dword v[28:29], v35, off sc1
	v_fma_f32 v35, v31, -2.0, 1.0
	v_fma_f32 v28, -v35, v35, 1.0
	v_mul_f32_e32 v28, v129, v28
	v_add_f32_e32 v31, v34, v19
	v_cvt_pk_bf16_f32 v29, v28, s0
	v_mul_f32_e64 v27, v35, -v28
	v_add_f32_e32 v28, v31, v31
	v_mul_f32_e32 v28, 0x3fb8aa3b, v28
	v_exp_f32_e32 v38, v28
	v_cvt_pk_bf16_f32 v27, v27, s0
	ds_write_b16 v37, v27 offset:4352
	v_or_b32_e32 v28, 1, v30
	v_add_f32_e32 v27, 1.0, v38
	v_rcp_f32_e32 v27, v27
	ds_write_b16 v37, v29
	v_ashrrev_i32_e32 v29, 31, v28
	v_lshlrev_b64 v[28:29], 9, v[28:29]
	v_lshl_add_u64 v[28:29], v[32:33], 0, v[28:29]
	v_fma_f32 v27, v27, -2.0, 1.0
	global_store_dword v[28:29], v31, off sc1
	v_fma_f32 v28, -v27, v27, 1.0
	v_mul_f32_e32 v28, v129, v28
	v_cvt_pk_bf16_f32 v29, v28, s0
	v_add_f32_e32 v31, v34, v20
	ds_write_b16 v37, v29 offset:272
	v_add_f32_e32 v29, v31, v31
	v_mul_f32_e32 v29, 0x3fb8aa3b, v29
	v_exp_f32_e32 v38, v29
	v_mul_f32_e64 v28, v27, -v28
	v_cvt_pk_bf16_f32 v28, v28, s0
	ds_write_b16 v37, v28 offset:4624
	v_add_f32_e32 v38, 1.0, v38
	v_or_b32_e32 v28, 2, v30
	v_rcp_f32_e32 v38, v38
	v_ashrrev_i32_e32 v29, 31, v28
	v_lshlrev_b64 v[28:29], 9, v[28:29]
	v_lshl_add_u64 v[28:29], v[32:33], 0, v[28:29]
	global_store_dword v[28:29], v31, off sc1
	v_fma_f32 v28, v38, -2.0, 1.0
	v_fma_f32 v29, -v28, v28, 1.0
	v_mul_f32_e32 v29, v129, v29
	v_cvt_pk_bf16_f32 v31, v29, s0
	v_add_f32_e32 v34, v34, v21
	ds_write_b16 v37, v31 offset:544
	v_add_f32_e32 v31, v34, v34
	v_mul_f32_e32 v31, 0x3fb8aa3b, v31
	v_exp_f32_e32 v38, v31
	v_mul_f32_e64 v29, v28, -v29
	v_cvt_pk_bf16_f32 v29, v29, s0
	ds_write_b16 v37, v29 offset:4896
	v_add_f32_e32 v29, 1.0, v38
	v_rcp_f32_e32 v29, v29
	v_or_b32_e32 v30, 3, v30
	v_ashrrev_i32_e32 v31, 31, v30
	v_lshlrev_b64 v[30:31], 9, v[30:31]
	v_lshl_add_u64 v[30:31], v[32:33], 0, v[30:31]
	v_fma_f32 v29, v29, -2.0, 1.0
	global_store_dword v[30:31], v34, off sc1
	v_fma_f32 v30, -v29, v29, 1.0
	v_mul_f32_e32 v30, v129, v30
	v_cvt_pk_bf16_f32 v31, v30, s0
	v_mul_f32_e64 v30, v29, -v30
	v_cvt_pk_bf16_f32 v30, v30, s0
	ds_write_b16 v37, v30 offset:5168
	v_mov_b32_e32 v30, 0x1d800
	v_mul_f32_e32 v36, v129, v35
	v_lshl_or_b32 v32, v128, 6, v30
	v_mov_b32_e32 v30, v107
	ds_write_b16 v37, v31 offset:816
	v_mov_b32_e32 v31, 0
	v_mov_b32_dpp v30, v36 quad_perm:[1,0,3,2] row_mask:0xf bank_mask:0xf
	v_fmac_f32_e32 v30, v129, v35
	v_cmp_eq_u32_e32 vcc, 0, v1
	v_add_u32_e32 v26, v32, v26
	v_add_f32_dpp v30, v30, v30 quad_perm:[2,3,0,1] row_mask:0xf bank_mask:0xf bound_ctrl:1
	s_nop 1
	v_add_f32_dpp v30, v30, v30 row_half_mirror row_mask:0xf bank_mask:0xf bound_ctrl:1
	s_nop 1
	v_mov_b32_dpp v31, v30 row_mirror row_mask:0xf bank_mask:0xf
	s_and_saveexec_b64 s[4:5], vcc
	v_add_f32_e32 v30, v30, v31
	ds_write_b32 v26, v30
	s_or_b64 exec, exec, s[4:5]
	v_mul_f32_e32 v30, v129, v27
	v_mov_b32_e32 v31, 0
	s_nop 1
	v_mov_b32_dpp v31, v30 quad_perm:[1,0,3,2] row_mask:0xf bank_mask:0xf
	v_fmac_f32_e32 v31, v129, v27
	s_nop 1
	v_add_f32_dpp v27, v31, v31 quad_perm:[2,3,0,1] row_mask:0xf bank_mask:0xf bound_ctrl:1
	s_nop 1
	v_add_f32_dpp v27, v27, v27 row_half_mirror row_mask:0xf bank_mask:0xf bound_ctrl:1
	s_nop 1
	v_mov_b32_dpp v107, v27 row_mirror row_mask:0xf bank_mask:0xf
	s_and_saveexec_b64 s[4:5], vcc
	v_add_f32_e32 v27, v27, v107
	ds_write_b32 v26, v27 offset:4
	s_or_b64 exec, exec, s[4:5]
	v_mul_f32_e32 v30, v129, v28
	v_mov_b32_e32 v31, 0
	v_mov_b32_e32 v27, 0
	s_nop 0
	v_mov_b32_dpp v31, v30 quad_perm:[1,0,3,2] row_mask:0xf bank_mask:0xf
	v_fmac_f32_e32 v31, v129, v28
	v_mov_b32_e32 v30, 0
	s_nop 0
	v_add_f32_dpp v28, v31, v31 quad_perm:[2,3,0,1] row_mask:0xf bank_mask:0xf bound_ctrl:1
	s_nop 1
	v_add_f32_dpp v28, v28, v28 row_half_mirror row_mask:0xf bank_mask:0xf bound_ctrl:1
	s_nop 1
	v_mov_b32_dpp v30, v28 row_mirror row_mask:0xf bank_mask:0xf
	s_and_saveexec_b64 s[4:5], vcc
	v_add_f32_e32 v28, v28, v30
	ds_write_b32 v26, v28 offset:8
	s_or_b64 exec, exec, s[4:5]
	v_mul_f32_e32 v28, v129, v29
	v_mov_b32_e32 v30, 0
	s_nop 1
	v_mov_b32_dpp v30, v28 quad_perm:[1,0,3,2] row_mask:0xf bank_mask:0xf
	v_fmac_f32_e32 v30, v129, v29
	s_nop 1
	v_add_f32_dpp v28, v30, v30 quad_perm:[2,3,0,1] row_mask:0xf bank_mask:0xf bound_ctrl:1
	s_nop 1
	v_add_f32_dpp v28, v28, v28 row_half_mirror row_mask:0xf bank_mask:0xf bound_ctrl:1
	s_nop 1
	v_mov_b32_dpp v27, v28 row_mirror row_mask:0xf bank_mask:0xf
	s_and_saveexec_b64 s[4:5], vcc
	v_add_f32_e32 v27, v28, v27
	ds_write_b32 v26, v27 offset:12
	s_or_b64 exec, exec, s[4:5]
	s_mov_b64 s[4:5], 0
.LBB0_24:
	s_and_b64 vcc, exec, s[4:5]
	s_cbranch_vccz .LBB0_28
	s_load_dwordx2 s[4:5], s[0:1], 0x68
	v_lshl_or_b32 v26, v24, 2, s12
	v_mov_b32_e32 v107, 0
	v_ashrrev_i32_e32 v27, 31, v26
	v_lshlrev_b64 v[28:29], 9, v[26:27]
	s_waitcnt lgkmcnt(0)
	v_lshl_add_u64 v[30:31], s[4:5], 0, v[106:107]
	v_lshl_add_u64 v[28:29], v[30:31], 0, v[28:29]
	v_mul_u32_u24_e32 v24, 0x440, v24
	s_mov_b32 s4, 0x19200
	global_store_dword v[28:29], v18, off sc1
	v_add3_u32 v28, v24, v25, s4
	v_mul_f32_e32 v24, v18, v18
	v_cvt_pk_bf16_f32 v27, v18, s0
	v_cvt_pk_bf16_f32 v24, v24, s0
	ds_write_b16 v28, v27
	ds_write_b16 v28, v24 offset:4352
	v_max3_f32 v27, |v18|, 0, |v19|
	v_or_b32_e32 v24, 1, v26
	v_cvt_pk_bf16_f32 v18, v19, s0
	v_ashrrev_i32_e32 v25, 31, v24
	ds_write_b16 v28, v18 offset:272
	v_mul_f32_e32 v18, v19, v19
	v_lshlrev_b64 v[24:25], 9, v[24:25]
	v_cvt_pk_bf16_f32 v18, v18, s0
	v_lshl_add_u64 v[24:25], v[30:31], 0, v[24:25]
	ds_write_b16 v28, v18 offset:4624
	v_or_b32_e32 v18, 2, v26
	global_store_dword v[24:25], v19, off sc1
	v_ashrrev_i32_e32 v19, 31, v18
	v_lshlrev_b64 v[18:19], 9, v[18:19]
	v_lshl_add_u64 v[18:19], v[30:31], 0, v[18:19]
	global_store_dword v[18:19], v20, off sc1
	v_cvt_pk_bf16_f32 v18, v20, s0
	ds_write_b16 v28, v18 offset:544
	v_mul_f32_e32 v18, v20, v20
	v_cvt_pk_bf16_f32 v18, v18, s0
	ds_write_b16 v28, v18 offset:4896
	v_or_b32_e32 v18, 3, v26
	v_ashrrev_i32_e32 v19, 31, v18
	v_lshlrev_b64 v[18:19], 9, v[18:19]
	v_lshl_add_u64 v[18:19], v[30:31], 0, v[18:19]
	global_store_dword v[18:19], v21, off sc1
	v_cvt_pk_bf16_f32 v18, v21, s0
	ds_write_b16 v28, v18 offset:816
	v_mul_f32_e32 v18, v21, v21
	v_cvt_pk_bf16_f32 v18, v18, s0
	v_max3_f32 v20, v27, |v20|, |v21|
	ds_write_b16 v28, v18 offset:5168
	v_mov_b32_e32 v18, v107
	v_mov_b32_e32 v19, v107
	v_cmp_eq_u32_e32 vcc, 0, v126
	v_mov_b32_dpp v18, v20 quad_perm:[1,0,3,2] row_mask:0xf bank_mask:0xf
	v_max_f32_e32 v18, v18, v18
	v_max_f32_e32 v18, v20, v18
	s_nop 1
	v_mov_b32_dpp v19, v18 quad_perm:[2,3,0,1] row_mask:0xf bank_mask:0xf
	v_max_f32_e32 v19, v19, v19
	v_max_f32_e32 v18, v18, v19
	v_mov_b32_e32 v19, v107
	s_nop 1
	v_mov_b32_dpp v19, v18 row_half_mirror row_mask:0xf bank_mask:0xf
	v_max_f32_e32 v19, v19, v19
	v_max_f32_e32 v18, v18, v19
	v_mov_b32_e32 v19, v107
	s_nop 1
	v_mov_b32_dpp v19, v18 row_mirror row_mask:0xf bank_mask:0xf
	v_max_f32_e32 v19, v19, v19
	v_max_f32_e32 v18, v18, v19
	s_nop 0
	v_readlane_b32 s8, v18, 0
	v_readlane_b32 s9, v18, 16
	v_readlane_b32 s10, v18, 32
	v_readlane_b32 s11, v18, 48
	v_and_b32_e32 v18, 0x7fffffff, v129
	s_nop 1
	v_add_f32_dpp v18, v18, |v129| quad_perm:[1,0,3,2] row_mask:0xf bank_mask:0xf bound_ctrl:1
	s_nop 1
	v_add_f32_dpp v18, v18, v18 quad_perm:[2,3,0,1] row_mask:0xf bank_mask:0xf bound_ctrl:1
	s_nop 1
	v_add_f32_dpp v18, v18, v18 row_half_mirror row_mask:0xf bank_mask:0xf bound_ctrl:1
	s_nop 1
	v_mov_b32_dpp v107, v18 row_mirror row_mask:0xf bank_mask:0xf
	s_and_saveexec_b64 s[4:5], vcc
	s_cbranch_execz .LBB0_27
	v_mov_b32_e32 v19, 0x1d800
	v_lshl_or_b32 v20, v128, 6, v19
	v_add_f32_e32 v19, v18, v107
	v_max_f32_e64 v18, s11, s11
	v_max_f32_e64 v21, s10, s10
	v_max_f32_e32 v18, v21, v18
	v_mov_b32_e32 v21, s9
	v_max3_f32 v18, s8, v21, v18
	ds_write_b64 v20, v[18:19]

.LBB0_28:
	s_mov_b64 s[8:9], -1
	s_and_b64 vcc, exec, s[6:7]
	s_waitcnt lgkmcnt(0)
	s_barrier
	s_cbranch_vccz .LBB0_34
	v_cmp_gt_u32_e32 vcc, 16, v0
	s_and_saveexec_b64 s[4:5], vcc
	s_cbranch_execz .LBB0_31
	v_or_b32_e32 v18, 0x1d800, v127
	v_add_u32_e32 v19, 0x1d840, v127
	v_add_u32_e32 v20, 0x1d880, v127
	v_add_u32_e32 v21, 0x1d8c0, v127
	v_add_u32_e32 v24, 0x1d900, v127
	v_add_u32_e32 v25, 0x1d940, v127
	v_add_u32_e32 v26, 0x1d980, v127
	v_add_u32_e32 v27, 0x1d9c0, v127
	ds_read_b32 v18, v18
	ds_read_b32 v19, v19
	ds_read_b32 v20, v20
	ds_read_b32 v21, v21
	ds_read_b32 v24, v24
	ds_read_b32 v25, v25
	ds_read_b32 v26, v26
	ds_read_b32 v27, v27
	s_waitcnt lgkmcnt(7)
	v_add_f32_e32 v18, 0, v18
	s_waitcnt lgkmcnt(6)
	v_add_f32_e32 v18, v18, v19
	s_waitcnt lgkmcnt(5)
	v_add_f32_e32 v18, v18, v20
	s_waitcnt lgkmcnt(4)
	v_add_f32_e32 v18, v18, v21
	s_load_dwordx2 s[6:7], s[0:1], 0x60
	s_waitcnt lgkmcnt(0)
	v_add_f32_e32 v18, v18, v24
	v_add_f32_e32 v18, v18, v25
	v_add_f32_e32 v18, v18, v26
	v_add_f32_e32 v20, v18, v27
	v_or_b32_e32 v18, s3, v0
	v_ashrrev_i32_e32 v19, 31, v18
	v_lshl_add_u64 v[18:19], v[18:19], 2, s[6:7]
	global_store_dword v[18:19], v20, off sc1
.LBB0_31:
	s_or_b64 exec, exec, s[4:5]
	s_movk_i32 s4, 0x200
	v_cmp_gt_u32_e32 vcc, s4, v0
	s_and_saveexec_b64 s[4:5], vcc
	s_cbranch_execz .LBB0_33
	s_load_dwordx2 s[6:7], s[0:1], 0x58
	s_ashr_i32 s3, s3, 9
	v_lshrrev_b32_e32 v20, 8, v0
	v_and_or_b32 v18, s3, -2, v20
	v_ashrrev_i32_e32 v19, 31, v18
	v_lshlrev_b64 v[18:19], 18, v[18:19]
	s_lshl_b32 s3, s2, 12
	s_waitcnt lgkmcnt(0)
	v_lshl_add_u64 v[18:19], s[6:7], 0, v[18:19]
	s_and_b32 s6, s3, 0x3f000
	s_mov_b32 s7, 0
	v_lshl_add_u64 v[24:25], v[18:19], 0, s[6:7]
	v_mul_u32_u24_e32 v18, 0x1100, v20
	s_movk_i32 s3, 0x110
	v_mad_u32_u24 v18, v1, s3, v18
	v_and_b32_e32 v19, 0xf0, v0
	s_mov_b32 s3, 0x19200
	v_add3_u32 v18, v18, v19, s3
	ds_read_b128 v[18:21], v18
	v_mov_b32_e32 v26, 4
	v_lshlrev_b32_sdwa v26, v26, v0 dst_sel:DWORD dst_unused:UNUSED_PAD src0_sel:DWORD src1_sel:BYTE_0
	v_mov_b32_e32 v27, 0
	v_lshl_add_u64 v[24:25], v[24:25], 0, v[26:27]
	s_waitcnt lgkmcnt(0)
	global_store_dwordx4 v[24:25], v[18:21], off sc1

.LBB0_34:
	s_load_dwordx2 s[4:5], s[0:1], 0x80
	s_and_b64 vcc, exec, s[8:9]
	s_cbranch_vccz .LBB0_40
	v_cmp_eq_u32_e32 vcc, 0, v0
	s_and_saveexec_b64 s[6:7], vcc
	s_cbranch_execz .LBB0_37
	v_mov_b32_e32 v18, 0x1d800
	v_mov_b32_e32 v20, 0x1d840
	ds_read_b64 v[18:19], v18
	ds_read_b64 v[20:21], v20
	v_mov_b32_e32 v24, 0x1d880
	v_mov_b32_e32 v26, 0x1d8c0
	ds_read_b64 v[24:25], v24
	ds_read_b64 v[26:27], v26
	s_waitcnt lgkmcnt(0)
	v_max_f32_e32 v18, v18, v18
	v_max_f32_e32 v20, v20, v20
	v_max_f32_e32 v18, v18, v20
	v_add_f32_e32 v19, v19, v21
	v_add_f32_e32 v19, v19, v25
	v_max3_f32 v21, v18, v24, v26
	v_mov_b32_e32 v18, 0x1d900
	v_add_f32_e32 v30, v19, v27
	v_mov_b32_e32 v19, 0x1d940
	v_mov_b32_e32 v20, 0x1d980
	ds_read_b64 v[24:25], v18
	ds_read_b64 v[26:27], v19
	ds_read_b64 v[28:29], v20
	v_mov_b32_e32 v18, 0x1d9c0
	ds_read_b96 v[18:20], v18
	s_mov_b32 s10, 0x3b800000
	s_waitcnt lgkmcnt(2)
	v_max3_f32 v21, v21, v24, v26
	s_waitcnt lgkmcnt(0)
	v_add_f32_e32 v20, v30, v25
	s_mov_b32 s11, 0x3eaab368
	v_max3_f32 v24, v21, v28, v18
	v_mul_f32_e32 v25, v24, v24
	v_add_f32_e32 v20, v20, v27
	v_pk_mul_f32 v[26:27], v[24:25], s[10:11]
	v_add_f32_e32 v20, v20, v29
	v_mov_b32_e32 v28, v26
	v_mul_f32_e32 v21, 0x3ec51eb8, v25
	v_mov_b32_e32 v18, v19
	v_mov_b32_e32 v19, v26
	v_fmac_f32_e32 v28, v24, v27
	v_pk_add_f32 v[18:19], v[20:21], v[18:19]
	s_mov_b32 s3, 0x3a83126f
	v_mul_f32_e32 v20, v18, v28
	s_load_dwordx2 s[8:9], s[0:1], 0x78
	v_cmp_nge_f32_e32 vcc, s3, v20
	v_mul_f32_e32 v18, v18, v19
	s_and_b64 s[10:11], vcc, exec
	v_cmp_nge_f32_e32 vcc, s3, v18
	s_cselect_b32 s12, 3, 2
	s_and_b64 s[10:11], vcc, exec
	s_cselect_b32 s12, s12, 1
	s_ashr_i32 s3, s2, 31
	s_lshl_b64 s[10:11], s[2:3], 2
	s_waitcnt lgkmcnt(0)
	s_add_u32 s8, s8, s10
	s_addc_u32 s9, s9, s11
	v_mov_b32_e32 v18, 0
	v_mov_b32_e32 v19, s12
	global_store_dword v18, v19, s[8:9] sc1
.LBB0_37:
	s_or_b64 exec, exec, s[6:7]
	s_movk_i32 s3, 0x200
	v_cmp_gt_u32_e32 vcc, s3, v0
	s_and_saveexec_b64 s[6:7], vcc
	s_cbranch_execz .LBB0_39
	v_lshrrev_b32_e32 v18, 4, v0
	v_bfe_u32 v18, v18, 3, 1
	s_load_dwordx2 s[0:1], s[0:1], 0x50
	v_lshl_or_b32 v18, s2, 1, v18
	v_lshrrev_b32_e32 v21, 8, v0
	v_ashrrev_i32_e32 v19, 31, v18
	v_lshlrev_b32_e32 v24, 10, v21
	v_mov_b32_e32 v25, 0
	v_lshl_add_u64 v[18:19], v[18:19], 2, v[24:25]
	v_lshrrev_b32_e32 v24, 2, v1
	v_or_b32_e32 v18, v18, v24
	v_bfe_u32 v20, v0, 4, 4
	v_lshlrev_b64 v[18:19], 9, v[18:19]
	s_waitcnt lgkmcnt(0)
	v_lshl_add_u64 v[26:27], s[0:1], 0, v[18:19]
	v_mul_u32_u24_e32 v18, 0x110, v20
	s_movk_i32 s0, 0x1100
	v_mad_u32_u24 v18, v21, s0, v18
	v_lshlrev_b32_e32 v1, 4, v1
	s_mov_b32 s0, 0x19200
	v_add3_u32 v1, v18, v1, s0
	ds_read_b128 v[18:21], v1
	v_lshlrev_b32_e32 v24, 7, v0
	v_and_b32_e32 v24, 0x180, v24
	v_lshl_add_u64 v[26:27], v[26:27], 0, v[24:25]
	v_and_b32_e32 v24, 0x70, v0
	v_lshl_add_u64 v[0:1], v[26:27], 0, v[24:25]
	s_waitcnt lgkmcnt(0)
	global_store_dwordx4 v[0:1], v[18:21], off sc1

.LBB0_40:
	s_waitcnt vmcnt(3)
	v_cmp_ne_u32_e32 vcc, 0, v14
	s_nop 1
	v_cndmask_b32_e64 v0, 0, 1, vcc
	v_cmp_eq_u32_e32 vcc, 0, v15
	s_nop 1
	v_cndmask_b32_e64 v1, 2, 0, vcc
	v_cmp_eq_u32_e32 vcc, 0, v16
	v_or_b32_e32 v0, v1, v0
	s_nop 0
	v_cndmask_b32_e64 v1, 4, 0, vcc
	v_cmp_eq_u32_e32 vcc, 0, v17
	s_nop 1
	v_cndmask_b32_e64 v14, 8, 0, vcc
	s_waitcnt vmcnt(2)
	v_cmp_eq_u32_e32 vcc, 0, v10
	v_bitop3_b16 v0, v0, v14, v1 bitop3:0xfe
	s_nop 0
	v_cndmask_b32_e64 v1, 16, 0, vcc
	v_cmp_eq_u32_e32 vcc, 0, v11
	s_nop 1
	v_cndmask_b32_e64 v10, 32, 0, vcc
	v_cmp_eq_u32_e32 vcc, 0, v12
	s_nop 1
	v_cndmask_b32_e64 v11, 64, 0, vcc
	v_bitop3_b16 v1, v1, v11, v10 bitop3:0xfe
	v_mov_b32_e32 v10, 0x80
	v_cmp_eq_u32_e32 vcc, 0, v13
	s_nop 1
	v_cndmask_b32_e64 v10, v10, 0, vcc
	v_bitop3_b16 v0, v1, v0, v10 bitop3:0xfe
	v_mov_b32_e32 v1, 0x100
	s_waitcnt vmcnt(1)
	v_cmp_eq_u32_e32 vcc, 0, v6
	v_mov_b32_e32 v6, 0x200
	s_nop 0
	v_cndmask_b32_e64 v1, v1, 0, vcc
	v_cmp_eq_u32_e32 vcc, 0, v7
	v_mov_b32_e32 v7, 0x400
	s_nop 0
	v_cndmask_b32_e64 v6, v6, 0, vcc
	v_cmp_eq_u32_e32 vcc, 0, v8
	s_nop 1
	v_cndmask_b32_e64 v7, v7, 0, vcc
	v_bitop3_b16 v1, v1, v7, v6 bitop3:0xfe
	v_mov_b32_e32 v6, 0x800
	v_cmp_eq_u32_e32 vcc, 0, v9
	s_nop 1
	v_cndmask_b32_e64 v6, v6, 0, vcc
	v_bitop3_b16 v0, v1, v0, v6 bitop3:0xfe
	v_mov_b32_e32 v1, 0x1000
	s_waitcnt vmcnt(0)
	v_cmp_eq_u32_e32 vcc, 0, v2
	v_mov_b32_e32 v2, 0x2000
	s_nop 0
	v_cndmask_b32_e64 v1, v1, 0, vcc
	v_cmp_eq_u32_e32 vcc, 0, v3
	v_mov_b32_e32 v3, 0x4000
	s_nop 0
	v_cndmask_b32_e64 v2, v2, 0, vcc
	v_cmp_eq_u32_e32 vcc, 0, v4
	s_nop 1
	v_cndmask_b32_e64 v3, v3, 0, vcc
	v_bitop3_b16 v1, v1, v3, v2 bitop3:0xfe
	v_mov_b32_e32 v2, 0xffff8000
	v_cmp_eq_u32_e32 vcc, 0, v5
	v_mov_b32_e32 v3, 0
	s_nop 0
	v_cndmask_b32_e64 v2, v2, 0, vcc
	v_bitop3_b16 v4, v1, v0, v2 bitop3:0xfe
	v_lshlrev_b64 v[0:1], 7, v[22:23]
	s_waitcnt lgkmcnt(0)
	v_lshl_add_u64 v[0:1], s[4:5], 0, v[0:1]
	v_lshlrev_b32_e32 v2, 1, v126
	v_lshl_add_u64 v[0:1], v[0:1], 0, v[2:3]
	global_store_short v[0:1], v4, off sc1
	s_endpgm

.LBB1_4:
	s_movk_i32 s5, 0x1010
	v_mad_u32_u24 v0, v73, s5, v56
	s_waitcnt lgkmcnt(0)
	s_barrier
	ds_read_b128 v[18:21], v0
	s_waitcnt vmcnt(3)
	v_pk_add_f32 v[22:23], s[4:5], v[16:17] op_sel_hi:[0,1]
	v_pk_add_f32 v[24:25], s[4:5], v[14:15] op_sel_hi:[0,1]
	ds_read_b128 v[14:17], v0 offset:1024
	s_waitcnt vmcnt(2)
	v_pk_add_f32 v[12:13], s[4:5], v[12:13] op_sel_hi:[0,1]
	s_waitcnt lgkmcnt(1)
	v_pk_add_f32 v[22:23], v[20:21], v[22:23]
	v_pk_add_f32 v[24:25], v[18:19], v[24:25]
	v_pk_add_f32 v[10:11], s[4:5], v[10:11] op_sel_hi:[0,1]
	v_cndmask_b32_e64 v21, v21, v23, s[2:3]
	v_cndmask_b32_e64 v20, v20, v22, s[2:3]
	v_cndmask_b32_e64 v22, v19, v25, s[2:3]
	v_cndmask_b32_e64 v23, v18, v24, s[2:3]
	s_waitcnt lgkmcnt(0)
	v_pk_add_f32 v[12:13], v[16:17], v[12:13]
	v_pk_add_f32 v[18:19], v[14:15], v[10:11]
	v_cndmask_b32_e64 v24, v17, v13, s[2:3]
	v_cndmask_b32_e64 v25, v16, v12, s[2:3]
	v_cndmask_b32_e64 v19, v15, v19, s[2:3]
	ds_read_b128 v[10:13], v0 offset:2048
	v_cndmask_b32_e64 v18, v14, v18, s[2:3]
	s_waitcnt vmcnt(1)
	v_pk_add_f32 v[14:15], s[4:5], v[8:9] op_sel_hi:[0,1]
	v_pk_add_f32 v[16:17], s[4:5], v[6:7] op_sel_hi:[0,1]
	ds_read_b128 v[6:9], v0 offset:3072
	s_waitcnt vmcnt(0)
	v_pk_add_f32 v[4:5], s[4:5], v[4:5] op_sel_hi:[0,1]
	v_cmp_ne_u16_e32 vcc, 0, v72
	s_cmp_lg_u64 vcc, 0
	v_and_b32_e32 v26, 0xffff, v72
	s_waitcnt lgkmcnt(0)
	v_pk_add_f32 v[4:5], v[8:9], v[4:5]
	s_cselect_b64 vcc, -1, 0
	v_cndmask_b32_e64 v4, v8, v4, s[2:3]
	v_mov_b32_e32 v8, 0xffff
	v_pk_add_f32 v[14:15], v[12:13], v[14:15]
	v_cndmask_b32_e32 v8, v8, v26, vcc
	v_cndmask_b32_e64 v0, v13, v15, s[2:3]
	v_and_b32_e32 v13, 1, v8
	v_pk_add_f32 v[16:17], v[10:11], v[16:17]
	v_cndmask_b32_e64 v12, v12, v14, s[2:3]
	v_cndmask_b32_e64 v5, v9, v5, s[2:3]
	v_mul_f32_e32 v9, 0x3fb8aa3b, v23
	v_mov_b32_e32 v14, 0xff800000
	v_cmp_eq_u32_e32 vcc, 1, v13
	v_and_b32_e32 v15, 2, v8
	v_cndmask_b32_e64 v11, v11, v17, s[2:3]
	v_cndmask_b32_e32 v9, v14, v9, vcc
	v_mul_f32_e32 v13, 0x3fb8aa3b, v22
	v_cmp_ne_u32_e32 vcc, 0, v15
	v_and_b32_e32 v17, 4, v8
	v_cndmask_b32_e64 v10, v10, v16, s[2:3]
	v_cndmask_b32_e32 v13, v14, v13, vcc
	v_mul_f32_e32 v16, 0x3fb8aa3b, v20
	v_cmp_ne_u32_e32 vcc, 0, v17
	v_and_b32_e32 v20, 8, v8
	v_mul_f32_e32 v17, 0x3fb8aa3b, v21
	v_cndmask_b32_e32 v16, v14, v16, vcc
	v_cmp_ne_u32_e32 vcc, 0, v20
	v_and_b32_e32 v20, 16, v8
	v_pk_add_f32 v[2:3], s[4:5], v[2:3] op_sel_hi:[0,1]
	v_cndmask_b32_e32 v17, v14, v17, vcc
	v_mul_f32_e32 v18, 0x3fb8aa3b, v18
	v_cmp_ne_u32_e32 vcc, 0, v20
	v_and_b32_e32 v20, 32, v8
	v_pk_add_f32 v[2:3], v[6:7], v[2:3]
	v_cndmask_b32_e32 v18, v14, v18, vcc
	v_mul_f32_e32 v19, 0x3fb8aa3b, v19
	v_cmp_ne_u32_e32 vcc, 0, v20
	v_and_b32_e32 v21, 64, v8
	v_cndmask_b32_e64 v7, v7, v3, s[2:3]
	v_cndmask_b32_e64 v6, v6, v2, s[2:3]
	v_lshlrev_b64 v[2:3], 12, v[54:55]
	v_cndmask_b32_e32 v19, v14, v19, vcc
	v_mul_f32_e32 v20, 0x3fb8aa3b, v25
	v_cmp_ne_u32_e32 vcc, 0, v21
	v_and_b32_e32 v22, 0x80, v8
	v_lshl_add_u64 v[2:3], s[0:1], 0, v[2:3]
	s_mov_b32 s0, 0xff800000
	v_cndmask_b32_e32 v20, v14, v20, vcc
	v_mul_f32_e32 v21, 0x3fb8aa3b, v24
	v_cmp_ne_u32_e32 vcc, 0, v22
	v_and_b32_e32 v22, 0x100, v8
	v_max3_f32 v15, v9, s0, v13
	v_cndmask_b32_e32 v21, v14, v21, vcc
	v_mul_f32_e32 v10, 0x3fb8aa3b, v10
	v_cmp_ne_u32_e32 vcc, 0, v22
	v_max3_f32 v15, v15, v16, v17
	v_max3_f32 v15, v15, v18, v19
	v_cndmask_b32_e32 v22, v14, v10, vcc
	v_mul_f32_e32 v10, 0x3fb8aa3b, v11
	v_and_b32_e32 v11, 0x200, v8
	v_cmp_ne_u32_e32 vcc, 0, v11
	v_mul_f32_e32 v11, 0x3fb8aa3b, v12
	v_and_b32_e32 v12, 0x400, v8
	v_max3_f32 v15, v15, v20, v21
	v_cndmask_b32_e32 v23, v14, v10, vcc
	v_cmp_ne_u32_e32 vcc, 0, v12
	v_max3_f32 v10, v15, v22, v23
	v_mul_f32_e32 v0, 0x3fb8aa3b, v0
	v_cndmask_b32_e32 v15, v14, v11, vcc
	v_and_b32_e32 v11, 0x800, v8
	v_cmp_ne_u32_e32 vcc, 0, v11
	v_and_b32_e32 v11, 0x1000, v8
	v_mul_f32_e32 v6, 0x3fb8aa3b, v6
	v_cndmask_b32_e32 v0, v14, v0, vcc
	v_cmp_ne_u32_e32 vcc, 0, v11
	v_mul_f32_e32 v4, 0x3fb8aa3b, v4
	s_movk_i32 s0, 0x7fff
	v_cndmask_b32_e32 v24, v14, v6, vcc
	v_mul_f32_e32 v6, 0x3fb8aa3b, v7
	v_and_b32_e32 v7, 0x2000, v8
	v_cmp_ne_u32_e32 vcc, 0, v7
	v_and_b32_e32 v7, 0x4000, v8
	v_max3_f32 v10, v10, v15, v0
	v_cndmask_b32_e32 v25, v14, v6, vcc
	v_cmp_ne_u32_e32 vcc, 0, v7
	v_max3_f32 v6, v10, v24, v25
	s_nop 0
	v_cndmask_b32_e32 v26, v14, v4, vcc
	v_mul_f32_e32 v4, 0x3fb8aa3b, v5
	v_cmp_lt_u32_e32 vcc, s0, v8
	v_mov_b32_e32 v5, 0
	s_nop 0
	v_cndmask_b32_e32 v27, v14, v4, vcc
	v_max3_f32 v4, v6, v26, v27
	s_nop 1
	v_mov_b32_dpp v5, v4 quad_perm:[1,0,3,2] row_mask:0xf bank_mask:0xf
	v_max_f32_e32 v5, v5, v5
	v_max_f32_e32 v4, v4, v5
	v_mov_b32_e32 v5, 0
	s_nop 1
	v_mov_b32_dpp v5, v4 quad_perm:[2,3,0,1] row_mask:0xf bank_mask:0xf
	v_max_f32_e32 v5, v5, v5
	v_max_f32_e32 v4, v4, v5
	v_mov_b32_e32 v5, 0
	s_nop 1
	v_mov_b32_dpp v5, v4 row_half_mirror row_mask:0xf bank_mask:0xf
	v_max_f32_e32 v5, v5, v5
	v_max_f32_e32 v4, v4, v5
	v_mov_b32_e32 v5, 0
	s_nop 1
	v_mov_b32_dpp v5, v4 row_mirror row_mask:0xf bank_mask:0xf
	v_max_f32_e32 v5, v5, v5
	v_max_f32_e32 v4, v4, v5
	s_nop 0
	v_readlane_b32 s2, v4, 32
	v_readlane_b32 s3, v4, 48
	v_readlane_b32 s0, v4, 0
	v_readlane_b32 s1, v4, 16
	v_max_f32_e64 v4, s3, s3
	v_max_f32_e64 v5, s2, s2
	v_max_f32_e32 v4, v5, v4
	v_mov_b32_e32 v5, s1
	v_max3_f32 v28, s0, v5, v4
	v_sub_f32_e32 v4, v9, v28
	v_exp_f32_e32 v4, v4
	v_sub_f32_e32 v5, v13, v28
	v_exp_f32_e32 v5, v5
	v_sub_f32_e32 v6, v16, v28
	v_exp_f32_e32 v6, v6
	v_sub_f32_e32 v7, v17, v28
	v_exp_f32_e32 v7, v7
	v_add_f32_e32 v8, 0, v4
	v_add_f32_e32 v8, v8, v5
	v_add_f32_e32 v8, v8, v6
	v_add_f32_e32 v12, v8, v7
	v_sub_f32_e32 v8, v18, v28
	v_exp_f32_e32 v8, v8
	v_sub_f32_e32 v9, v19, v28
	v_exp_f32_e32 v9, v9
	v_sub_f32_e32 v10, v20, v28
	v_exp_f32_e32 v10, v10
	v_sub_f32_e32 v11, v21, v28
	v_exp_f32_e32 v11, v11
	v_add_f32_e32 v12, v12, v8
	v_add_f32_e32 v12, v12, v9
	v_add_f32_e32 v12, v12, v10
	v_add_f32_e32 v16, v12, v11
	v_sub_f32_e32 v12, v22, v28
	v_exp_f32_e32 v12, v12
	v_sub_f32_e32 v13, v23, v28
	v_exp_f32_e32 v13, v13
	v_sub_f32_e32 v14, v15, v28
	v_exp_f32_e32 v14, v14
	v_sub_f32_e32 v0, v0, v28
	v_exp_f32_e32 v15, v0
	v_add_f32_e32 v0, v16, v12
	v_sub_f32_e32 v16, v24, v28
	v_exp_f32_e32 v16, v16
	v_sub_f32_e32 v17, v25, v28
	v_add_f32_e32 v0, v0, v13
	v_exp_f32_e32 v17, v17
	v_sub_f32_e32 v18, v26, v28
	v_add_f32_e32 v0, v0, v14
	v_exp_f32_e32 v18, v18
	v_sub_f32_e32 v19, v27, v28
	v_add_f32_e32 v0, v0, v15
	v_exp_f32_e32 v19, v19
	v_add_f32_e32 v0, v0, v16
	v_add_f32_e32 v0, v0, v17
	v_add_f32_e32 v0, v0, v18
	v_add_f32_e32 v0, v0, v19
	s_nop 1
	v_add_f32_dpp v0, v0, v0 quad_perm:[1,0,3,2] row_mask:0xf bank_mask:0xf bound_ctrl:1
	s_nop 1
	v_add_f32_dpp v0, v0, v0 quad_perm:[2,3,0,1] row_mask:0xf bank_mask:0xf bound_ctrl:1
	s_nop 1
	v_add_f32_dpp v0, v0, v0 row_half_mirror row_mask:0xf bank_mask:0xf bound_ctrl:1
	s_nop 1
	v_add_f32_dpp v0, v0, v0 row_mirror row_mask:0xf bank_mask:0xf bound_ctrl:1
	s_nop 0
	v_readlane_b32 s2, v0, 16
	v_readlane_b32 s3, v0, 48
	v_readlane_b32 s0, v0, 0
	v_readlane_b32 s1, v0, 32
	v_mov_b32_e32 v20, s2
	v_mov_b32_e32 v21, s3
	v_pk_add_f32 v[20:21], s[0:1], v[20:21]
	s_nop 0
	v_add_f32_e32 v0, v20, v21
	v_div_scale_f32 v22, s[0:1], v0, v0, 1.0
	v_rcp_f32_e32 v23, v22
	v_lshlrev_b32_e32 v20, 2, v1
	v_mov_b32_e32 v21, 0
	v_lshl_add_u64 v[20:21], v[2:3], 0, v[20:21]
	v_fma_f32 v1, -v22, v23, 1.0
	v_fmac_f32_e32 v23, v1, v23
	v_div_scale_f32 v1, vcc, 1.0, v0, 1.0
	v_mul_f32_e32 v2, v1, v23
	v_fma_f32 v3, -v22, v2, v1
	v_fmac_f32_e32 v2, v3, v23
	v_fma_f32 v1, -v22, v2, v1
	v_div_fmas_f32 v1, v1, v23, v2
	v_div_fixup_f32 v22, v1, v0, 1.0
	v_pk_mul_f32 v[2:3], v[22:23], v[6:7] op_sel_hi:[0,1]
	v_pk_mul_f32 v[0:1], v[22:23], v[4:5] op_sel_hi:[0,1]
	global_store_dwordx4 v[20:21], v[0:3], off sc1
	s_nop 1
	v_pk_mul_f32 v[2:3], v[22:23], v[10:11] op_sel_hi:[0,1]
	v_pk_mul_f32 v[0:1], v[22:23], v[8:9] op_sel_hi:[0,1]
	global_store_dwordx4 v[20:21], v[0:3], off offset:1024 sc1
	s_nop 1
	v_pk_mul_f32 v[2:3], v[22:23], v[14:15] op_sel_hi:[0,1]
	v_pk_mul_f32 v[0:1], v[22:23], v[12:13] op_sel_hi:[0,1]
	global_store_dwordx4 v[20:21], v[0:3], off offset:2048 sc1
	s_nop 1
	v_pk_mul_f32 v[2:3], v[22:23], v[18:19] op_sel_hi:[0,1]
	v_pk_mul_f32 v[0:1], v[22:23], v[16:17] op_sel_hi:[0,1]
	global_store_dwordx4 v[20:21], v[0:3], off offset:3072 sc1
	s_endpgm
